# speedup vs baseline: 1.0085x; 1.0052x over previous
.LBB2_127:
	s_or_b64 exec, exec, s[8:9]
	v_mbcnt_lo_u32_b32 v3, -1, 0
	v_mbcnt_hi_u32_b32 v3, -1, v3
	v_and_b32_e32 v4, 64, v3
	v_add_u32_e32 v4, 64, v4
	v_xor_b32_e32 v5, 32, v3
	v_cmp_lt_i32_e32 vcc, v5, v4
	v_xor_b32_e32 v6, 16, v3
	s_nop 0
	v_cndmask_b32_e32 v5, v3, v5, vcc
	v_lshlrev_b32_e32 v5, 2, v5
	v_mov_b32_e32 v5, v2
	s_nop 1
	v_permlane32_swap_b32_e32 v2, v5
	v_max_f32_e32 v2, v2, v2
	v_cmp_lt_i32_e32 vcc, v6, v4
	s_waitcnt lgkmcnt(0)
	v_max_f32_e32 v5, v5, v5
	v_max_f32_e32 v2, v2, v5
	v_cndmask_b32_e32 v5, v3, v6, vcc
	v_lshlrev_b32_e32 v5, 2, v5
	v_mov_b32_e32 v5, v2
	s_nop 1
	v_permlane16_swap_b32_e32 v2, v5
	v_xor_b32_e32 v6, 8, v3
	v_cmp_lt_i32_e32 vcc, v6, v4
	s_waitcnt lgkmcnt(0)
	v_max_f32_e32 v5, v5, v5
	v_max_f32_e32 v2, v2, v5
	v_cndmask_b32_e32 v5, v3, v6, vcc
	v_lshlrev_b32_e32 v5, 2, v5
	s_nop 1
	v_mov_b32_dpp v5, v2 row_ror:8 row_mask:0xf bank_mask:0xf
	v_xor_b32_e32 v6, 4, v3
	v_cmp_lt_i32_e32 vcc, v6, v4
	s_waitcnt lgkmcnt(0)
	v_max_f32_e32 v5, v5, v5
	v_max_f32_e32 v2, v2, v5
	v_cndmask_b32_e32 v5, v3, v6, vcc
	v_lshlrev_b32_e32 v5, 2, v5
	s_nop 1
	v_mov_b32_dpp v5, v2 row_ror:4 row_mask:0xf bank_mask:0xf
	v_xor_b32_e32 v6, 2, v3
	v_cmp_lt_i32_e32 vcc, v6, v4
	s_waitcnt lgkmcnt(0)
	v_max_f32_e32 v5, v5, v5
	v_max_f32_e32 v2, v2, v5
	v_cndmask_b32_e32 v5, v3, v6, vcc
	v_lshlrev_b32_e32 v5, 2, v5
	s_nop 1
	v_mov_b32_dpp v5, v2 row_ror:2 row_mask:0xf bank_mask:0xf
	v_xor_b32_e32 v6, 1, v3
	v_cmp_lt_i32_e32 vcc, v6, v4
	s_waitcnt lgkmcnt(0)
	v_max_f32_e32 v5, v5, v5
	v_cndmask_b32_e32 v3, v3, v6, vcc
	v_max_f32_e32 v2, v2, v5
	v_lshlrev_b32_e32 v3, 2, v3
	s_nop 1
	v_mov_b32_dpp v3, v2 row_ror:1 row_mask:0xf bank_mask:0xf
	v_cmp_eq_u32_e32 vcc, 0, v146
	s_and_b64 s[8:9], vcc, s[10:11]
	s_and_saveexec_b64 s[4:5], s[8:9]
	s_cbranch_execz .LBB2_129
	s_lshl_b32 s8, s20, 2
	s_waitcnt lgkmcnt(0)
	v_max_f32_e32 v3, v3, v3
	v_max_f32_e32 v2, v2, v2
	s_add_i32 s8, s8, 0x10800
	v_max_f32_e32 v2, v2, v3
	v_mov_b32_e32 v3, s8
	ds_write_b32 v3, v2
